# baseline (speedup 1.0000x reference)
.Lrnn_sk2:
	v_mfma_f32_16x16x32_f16 v[186:189], a[124:127], v[146:149], v[186:189]
	ds_read_b128 v[146:149], v241 offset:512
	s_waitcnt lgkmcnt(3)
	v_mfma_f32_16x16x32_f16 v[198:201], v[154:157], v[150:153], v[198:201]
	ds_read_b128 v[154:157], v213 offset:8192
	v_mfma_f32_16x16x32_f16 v[194:197], v[158:161], v[150:153], v[194:197]
	ds_read_b128 v[158:161], v213 offset:9216
	v_mfma_f32_16x16x32_f16 v[190:193], v[162:165], v[150:153], v[190:193]
	ds_read_b128 v[162:165], v213 offset:10240
	v_mfma_f32_16x16x32_f16 v[186:189], v[166:169], v[150:153], v[186:189]
	ds_read_b128 v[166:169], v213 offset:11264
	ds_read_b128 v[150:153], v241 offset:768
	s_waitcnt lgkmcnt(7)
	v_mfma_f32_16x16x32_f16 v[198:201], a[140:143], v[138:141], v[198:201]
	v_mfma_f32_16x16x32_f16 v[194:197], a[144:147], v[138:141], v[194:197]
	v_mfma_f32_16x16x32_f16 v[190:193], a[148:151], v[138:141], v[190:193]
	v_mfma_f32_16x16x32_f16 v[186:189], a[168:171], v[138:141], v[186:189]
	ds_read_b128 v[138:141], v242 offset:0
	s_waitcnt lgkmcnt(7)
	v_mfma_f32_16x16x32_f16 v[198:201], v[10:13], v[142:145], v[198:201]
	v_mfma_f32_16x16x32_f16 v[194:197], v[14:17], v[142:145], v[194:197]
	v_mfma_f32_16x16x32_f16 v[190:193], v[18:21], v[142:145], v[190:193]
	v_mfma_f32_16x16x32_f16 v[186:189], v[22:25], v[142:145], v[186:189]
	ds_read_b128 v[142:145], v243 offset:0
	s_waitcnt lgkmcnt(7)
	v_mfma_f32_16x16x32_f16 v[198:201], v[54:57], v[146:149], v[198:201]
	v_mfma_f32_16x16x32_f16 v[194:197], v[58:61], v[146:149], v[194:197]
	v_mfma_f32_16x16x32_f16 v[190:193], v[62:65], v[146:149], v[190:193]
	v_mfma_f32_16x16x32_f16 v[186:189], v[66:69], v[146:149], v[186:189]
	ds_read_b128 v[146:149], v242 offset:256
	s_waitcnt lgkmcnt(3)
	v_mfma_f32_16x16x32_f16 v[198:201], v[154:157], v[150:153], v[198:201]
	ds_read_b128 v[154:157], v213 offset:16384
	v_mfma_f32_16x16x32_f16 v[194:197], v[158:161], v[150:153], v[194:197]
	ds_read_b128 v[158:161], v213 offset:17408
	v_mfma_f32_16x16x32_f16 v[190:193], v[162:165], v[150:153], v[190:193]
	ds_read_b128 v[162:165], v213 offset:18432
	v_mfma_f32_16x16x32_f16 v[186:189], v[166:169], v[150:153], v[186:189]
	ds_read_b128 v[166:169], v213 offset:19456
	ds_read_b128 v[150:153], v242 offset:768
	s_waitcnt lgkmcnt(7)
	v_mfma_f32_16x16x32_f16 v[198:201], a[48:51], v[138:141], v[198:201]
	v_mfma_f32_16x16x32_f16 v[194:197], a[52:55], v[138:141], v[194:197]
	v_mfma_f32_16x16x32_f16 v[190:193], a[56:59], v[138:141], v[190:193]
	v_mfma_f32_16x16x32_f16 v[186:189], a[60:63], v[138:141], v[186:189]
	ds_read_b128 v[138:141], v243 offset:256
	s_waitcnt lgkmcnt(7)
	v_mfma_f32_16x16x32_f16 v[198:201], a[76:79], v[142:145], v[198:201]
	v_mfma_f32_16x16x32_f16 v[194:197], a[80:83], v[142:145], v[194:197]
	v_mfma_f32_16x16x32_f16 v[190:193], a[84:87], v[142:145], v[190:193]
	v_mfma_f32_16x16x32_f16 v[186:189], a[88:91], v[142:145], v[186:189]
	ds_read_b128 v[142:145], v242 offset:512
	s_waitcnt lgkmcnt(7)
	v_mfma_f32_16x16x32_f16 v[198:201], a[176:179], v[146:149], v[198:201]
	v_mfma_f32_16x16x32_f16 v[194:197], a[180:183], v[146:149], v[194:197]
	v_mfma_f32_16x16x32_f16 v[190:193], a[184:187], v[146:149], v[190:193]
	v_mfma_f32_16x16x32_f16 v[186:189], a[188:191], v[146:149], v[186:189]
	ds_read_b128 v[146:149], v243 offset:512
	s_waitcnt lgkmcnt(3)
	v_mfma_f32_16x16x32_f16 v[198:201], v[154:157], v[150:153], v[198:201]
	ds_read_b128 v[154:157], v213 offset:24576
	v_mfma_f32_16x16x32_f16 v[194:197], v[158:161], v[150:153], v[194:197]
	ds_read_b128 v[158:161], v213 offset:25600
	v_mfma_f32_16x16x32_f16 v[190:193], v[162:165], v[150:153], v[190:193]
	ds_read_b128 v[162:165], v213 offset:26624
	v_mfma_f32_16x16x32_f16 v[186:189], v[166:169], v[150:153], v[186:189]
	ds_read_b128 v[166:169], v213 offset:27648
	ds_read_b128 v[150:153], v243 offset:768
	s_waitcnt lgkmcnt(7)
	v_mfma_f32_16x16x32_f16 v[198:201], a[212:215], v[138:141], v[198:201]
	v_mfma_f32_16x16x32_f16 v[194:197], a[216:219], v[138:141], v[194:197]
	v_mfma_f32_16x16x32_f16 v[190:193], a[220:223], v[138:141], v[190:193]
	v_mfma_f32_16x16x32_f16 v[186:189], a[232:235], v[138:141], v[186:189]
	ds_read_b128 v[138:141], v240 offset:0
	s_waitcnt lgkmcnt(7)
	v_mfma_f32_16x16x32_f16 v[198:201], v[74:77], v[142:145], v[198:201]
	v_mfma_f32_16x16x32_f16 v[194:197], v[78:81], v[142:145], v[194:197]
	v_mfma_f32_16x16x32_f16 v[190:193], v[82:85], v[142:145], v[190:193]
	v_mfma_f32_16x16x32_f16 v[186:189], v[86:89], v[142:145], v[186:189]
	ds_read_b128 v[142:145], v241 offset:0
	s_waitcnt lgkmcnt(7)
	v_mfma_f32_16x16x32_f16 v[198:201], v[94:97], v[146:149], v[198:201]
	v_mfma_f32_16x16x32_f16 v[194:197], v[98:101], v[146:149], v[194:197]
	v_mfma_f32_16x16x32_f16 v[190:193], v[102:105], v[146:149], v[190:193]
	v_mfma_f32_16x16x32_f16 v[186:189], v[106:109], v[146:149], v[186:189]
	ds_read_b128 v[146:149], v240 offset:256
	s_waitcnt lgkmcnt(3)
	v_mfma_f32_16x16x32_f16 v[198:201], v[154:157], v[150:153], v[198:201]
	ds_read_b128 v[154:157], v213 offset:4096
	v_mfma_f32_16x16x32_f16 v[194:197], v[158:161], v[150:153], v[194:197]
	ds_read_b128 v[158:161], v213 offset:5120
	v_mfma_f32_16x16x32_f16 v[190:193], v[162:165], v[150:153], v[190:193]
	ds_read_b128 v[162:165], v213 offset:6144
	v_mfma_f32_16x16x32_f16 v[186:189], v[166:169], v[150:153], v[186:189]
	ds_read_b128 v[166:169], v213 offset:7168
	ds_read_b128 v[150:153], v240 offset:768
	s_waitcnt lgkmcnt(7)
	v_mfma_f32_16x16x32_f16 v[182:185], a[8:11], v[138:141], v[182:185]
	v_mfma_f32_16x16x32_f16 v[178:181], a[0:3], v[138:141], v[178:181]
	v_mfma_f32_16x16x32_f16 v[174:177], a[4:7], v[138:141], v[174:177]
	v_mfma_f32_16x16x32_f16 v[170:173], a[32:35], v[138:141], v[170:173]
	ds_read_b128 v[138:141], v241 offset:256
	s_waitcnt lgkmcnt(7)
	v_mfma_f32_16x16x32_f16 v[182:185], a[28:31], v[142:145], v[182:185]
	v_exp_f32_e32 v198, v198
	v_mfma_f32_16x16x32_f16 v[178:181], a[36:39], v[142:145], v[178:181]
	v_exp_f32_e32 v199, v199
	v_mfma_f32_16x16x32_f16 v[174:177], a[40:43], v[142:145], v[174:177]
	v_exp_f32_e32 v200, v200
	v_mfma_f32_16x16x32_f16 v[170:173], a[44:47], v[142:145], v[170:173]
	ds_read_b128 v[142:145], v240 offset:512
	v_exp_f32_e32 v201, v201
	s_waitcnt lgkmcnt(7)
	v_mfma_f32_16x16x32_f16 v[182:185], a[136:139], v[146:149], v[182:185]
	v_exp_f32_e32 v194, v194
	v_mfma_f32_16x16x32_f16 v[178:181], a[128:131], v[146:149], v[178:181]
	v_exp_f32_e32 v195, v195
	v_mfma_f32_16x16x32_f16 v[174:177], a[132:135], v[146:149], v[174:177]
	v_exp_f32_e32 v196, v196
	v_mfma_f32_16x16x32_f16 v[170:173], a[152:155], v[146:149], v[170:173]
	ds_read_b128 v[146:149], v241 offset:512
	v_exp_f32_e32 v197, v197
	s_waitcnt lgkmcnt(3)
	v_mfma_f32_16x16x32_f16 v[182:185], v[154:157], v[150:153], v[182:185]
	ds_read_b128 v[154:157], v213 offset:12288
	v_exp_f32_e32 v190, v190
	v_mfma_f32_16x16x32_f16 v[178:181], v[158:161], v[150:153], v[178:181]
	ds_read_b128 v[158:161], v213 offset:13312
	v_exp_f32_e32 v191, v191
	v_mfma_f32_16x16x32_f16 v[174:177], v[162:165], v[150:153], v[174:177]
	ds_read_b128 v[162:165], v213 offset:14336
	v_exp_f32_e32 v192, v192
	v_mfma_f32_16x16x32_f16 v[170:173], v[166:169], v[150:153], v[170:173]
	ds_read_b128 v[166:169], v213 offset:15360
	ds_read_b128 v[150:153], v241 offset:768
	v_exp_f32_e32 v193, v193
	s_waitcnt lgkmcnt(7)
	v_mfma_f32_16x16x32_f16 v[182:185], a[172:175], v[138:141], v[182:185]
	v_exp_f32_e32 v186, v186
	v_mfma_f32_16x16x32_f16 v[178:181], a[156:159], v[138:141], v[178:181]
	v_exp_f32_e32 v187, v187
	v_mfma_f32_16x16x32_f16 v[174:177], a[160:163], v[138:141], v[174:177]
	v_exp_f32_e32 v188, v188
	v_mfma_f32_16x16x32_f16 v[170:173], a[164:167], v[138:141], v[170:173]
	ds_read_b128 v[138:141], v242 offset:0
	v_exp_f32_e32 v189, v189
	s_waitcnt lgkmcnt(7)
	v_mfma_f32_16x16x32_f16 v[182:185], v[50:53], v[142:145], v[182:185]
	v_add_f32_e32 v198, 1.0, v198
	v_add_f32_e32 v199, 1.0, v199
	v_mfma_f32_16x16x32_f16 v[178:181], v[26:29], v[142:145], v[178:181]
	v_add_f32_e32 v200, 1.0, v200
	v_add_f32_e32 v201, 1.0, v201
	v_mfma_f32_16x16x32_f16 v[174:177], v[30:33], v[142:145], v[174:177]
	v_add_f32_e32 v194, 1.0, v194
	v_add_f32_e32 v195, 1.0, v195
	v_mfma_f32_16x16x32_f16 v[170:173], v[34:37], v[142:145], v[170:173]
	ds_read_b128 v[142:145], v243 offset:0
	v_add_f32_e32 v196, 1.0, v196
	v_add_f32_e32 v197, 1.0, v197
	s_waitcnt lgkmcnt(7)
	v_mfma_f32_16x16x32_f16 v[182:185], v[70:73], v[146:149], v[182:185]
	v_add_f32_e32 v190, 1.0, v190
	v_add_f32_e32 v191, 1.0, v191
	v_mfma_f32_16x16x32_f16 v[178:181], v[38:41], v[146:149], v[178:181]
	v_add_f32_e32 v192, 1.0, v192
	v_add_f32_e32 v193, 1.0, v193
	v_mfma_f32_16x16x32_f16 v[174:177], v[42:45], v[146:149], v[174:177]
	v_add_f32_e32 v186, 1.0, v186
	v_add_f32_e32 v187, 1.0, v187
	v_mfma_f32_16x16x32_f16 v[170:173], v[46:49], v[146:149], v[170:173]
	ds_read_b128 v[146:149], v242 offset:256
	v_add_f32_e32 v188, 1.0, v188
	v_add_f32_e32 v189, 1.0, v189
	s_waitcnt lgkmcnt(3)
	v_mfma_f32_16x16x32_f16 v[182:185], v[154:157], v[150:153], v[182:185]
	ds_read_b128 v[154:157], v213 offset:20480
	v_rcp_f32_e32 v198, v198
	v_mfma_f32_16x16x32_f16 v[178:181], v[158:161], v[150:153], v[178:181]
	ds_read_b128 v[158:161], v213 offset:21504
	v_rcp_f32_e32 v199, v199
	v_mfma_f32_16x16x32_f16 v[174:177], v[162:165], v[150:153], v[174:177]
	ds_read_b128 v[162:165], v213 offset:22528
	v_rcp_f32_e32 v200, v200
	v_mfma_f32_16x16x32_f16 v[170:173], v[166:169], v[150:153], v[170:173]
	ds_read_b128 v[166:169], v213 offset:23552
	ds_read_b128 v[150:153], v242 offset:768
	v_rcp_f32_e32 v201, v201
	s_waitcnt lgkmcnt(7)
	v_mfma_f32_16x16x32_f16 v[182:185], a[72:75], v[138:141], v[182:185]
	v_rcp_f32_e32 v194, v194
	v_mfma_f32_16x16x32_f16 v[178:181], a[64:67], v[138:141], v[178:181]
	v_rcp_f32_e32 v195, v195
	v_mfma_f32_16x16x32_f16 v[174:177], a[68:71], v[138:141], v[174:177]
	v_rcp_f32_e32 v196, v196
	v_mfma_f32_16x16x32_f16 v[170:173], a[96:99], v[138:141], v[170:173]
	ds_read_b128 v[138:141], v243 offset:256
	v_rcp_f32_e32 v197, v197
	s_waitcnt lgkmcnt(7)
	v_mfma_f32_16x16x32_f16 v[182:185], a[92:95], v[142:145], v[182:185]
	v_rcp_f32_e32 v190, v190
	v_mfma_f32_16x16x32_f16 v[178:181], a[100:103], v[142:145], v[178:181]
	v_rcp_f32_e32 v191, v191
	v_mfma_f32_16x16x32_f16 v[174:177], a[104:107], v[142:145], v[174:177]
	v_rcp_f32_e32 v192, v192
	v_mfma_f32_16x16x32_f16 v[170:173], a[108:111], v[142:145], v[170:173]
	ds_read_b128 v[142:145], v242 offset:512
	v_rcp_f32_e32 v193, v193
	s_waitcnt lgkmcnt(7)
	v_mfma_f32_16x16x32_f16 v[182:185], a[208:211], v[146:149], v[182:185]
	v_rcp_f32_e32 v186, v186
	v_mfma_f32_16x16x32_f16 v[178:181], a[224:227], v[146:149], v[178:181]
	v_rcp_f32_e32 v187, v187
	v_mfma_f32_16x16x32_f16 v[174:177], a[228:231], v[146:149], v[174:177]
	v_rcp_f32_e32 v188, v188
	v_mfma_f32_16x16x32_f16 v[170:173], a[240:243], v[146:149], v[170:173]
	ds_read_b128 v[146:149], v243 offset:512
	v_rcp_f32_e32 v189, v189
	s_waitcnt lgkmcnt(3)
	v_mfma_f32_16x16x32_f16 v[182:185], v[154:157], v[150:153], v[182:185]
	ds_read_b128 v[154:157], v213 offset:28672
	v_fma_f32 v198, v198, -2.0, 1.0
	v_fma_f32 v199, v199, -2.0, 1.0
	v_mfma_f32_16x16x32_f16 v[178:181], v[158:161], v[150:153], v[178:181]
	ds_read_b128 v[158:161], v213 offset:29696
	v_fma_f32 v200, v200, -2.0, 1.0
	v_fma_f32 v201, v201, -2.0, 1.0
	v_mfma_f32_16x16x32_f16 v[174:177], v[162:165], v[150:153], v[174:177]
	ds_read_b128 v[162:165], v213 offset:30720
	v_fma_f32 v194, v194, -2.0, 1.0
	v_fma_f32 v195, v195, -2.0, 1.0
	v_mfma_f32_16x16x32_f16 v[170:173], v[166:169], v[150:153], v[170:173]
	ds_read_b128 v[166:169], v213 offset:31744
	ds_read_b128 v[150:153], v243 offset:768
	v_fma_f32 v196, v196, -2.0, 1.0
	v_fma_f32 v197, v197, -2.0, 1.0
	s_waitcnt lgkmcnt(7)
	v_mfma_f32_16x16x32_f16 v[182:185], a[236:239], v[138:141], v[182:185]
	v_fma_f32 v190, v190, -2.0, 1.0
	v_fma_f32 v191, v191, -2.0, 1.0
	v_mfma_f32_16x16x32_f16 v[178:181], a[244:247], v[138:141], v[178:181]
	v_fma_f32 v192, v192, -2.0, 1.0
	v_fma_f32 v193, v193, -2.0, 1.0
	v_mfma_f32_16x16x32_f16 v[174:177], v[2:5], v[138:141], v[174:177]
	v_fma_f32 v186, v186, -2.0, 1.0
	v_fma_f32 v187, v187, -2.0, 1.0
	v_mfma_f32_16x16x32_f16 v[170:173], v[6:9], v[138:141], v[170:173]
	v_fma_f32 v188, v188, -2.0, 1.0
	v_fma_f32 v189, v189, -2.0, 1.0
	s_waitcnt lgkmcnt(6)
	v_mfma_f32_16x16x32_f16 v[182:185], v[90:93], v[142:145], v[182:185]
	v_cvt_pk_f16_f32 v198, v198, v199
	v_cvt_pk_f16_f32 v199, v200, v201
	v_mfma_f32_16x16x32_f16 v[178:181], v[114:117], v[142:145], v[178:181]
	v_cvt_pk_f16_f32 v194, v194, v195
	v_cvt_pk_f16_f32 v195, v196, v197
	v_mfma_f32_16x16x32_f16 v[174:177], v[118:121], v[142:145], v[174:177]
	v_cvt_pk_f16_f32 v190, v190, v191
	v_cvt_pk_f16_f32 v191, v192, v193
	v_mfma_f32_16x16x32_f16 v[170:173], v[122:125], v[142:145], v[170:173]
	v_cvt_pk_f16_f32 v186, v186, v187
	v_cvt_pk_f16_f32 v187, v188, v189
	s_waitcnt lgkmcnt(5)
	v_mfma_f32_16x16x32_f16 v[182:185], v[110:113], v[146:149], v[182:185]
	v_add_u32_e32 v244, s5, v217
	v_mfma_f32_16x16x32_f16 v[178:181], v[126:129], v[146:149], v[178:181]
	ds_write_b64 v244, v[198:199]
	v_mfma_f32_16x16x32_f16 v[174:177], v[130:133], v[146:149], v[174:177]
	v_add_u32_e32 v245, s5, v215
	v_mfma_f32_16x16x32_f16 v[170:173], v[134:137], v[146:149], v[170:173]
	ds_write_b64 v245, v[194:195]
	s_waitcnt lgkmcnt(2)
	v_mfma_f32_16x16x32_f16 v[182:185], v[154:157], v[150:153], v[182:185]
	v_add_u32_e32 v246, s5, v211
	v_mfma_f32_16x16x32_f16 v[178:181], v[158:161], v[150:153], v[178:181]
	ds_write_b64 v246, v[190:191]
	v_mfma_f32_16x16x32_f16 v[174:177], v[162:165], v[150:153], v[174:177]
	v_add_u32_e32 v247, s5, v212
	v_mfma_f32_16x16x32_f16 v[170:173], v[166:169], v[150:153], v[170:173]
	ds_write_b64 v247, v[186:187]
	ds_read_b128 v[154:157], v213 offset:0
	ds_read_b128 v[158:161], v213 offset:1024
	ds_read_b128 v[162:165], v213 offset:2048
	ds_read_b128 v[166:169], v213 offset:3072
	s_waitcnt vmcnt(2)
	v_cvt_f32_f16_e32 v198, v224
	v_cvt_f32_f16_sdwa v199, v224 dst_sel:DWORD dst_unused:UNUSED_PAD src0_sel:WORD_1
	v_cvt_f32_f16_e32 v200, v225
	v_cvt_f32_f16_sdwa v201, v225 dst_sel:DWORD dst_unused:UNUSED_PAD src0_sel:WORD_1
	v_cvt_f32_f16_e32 v194, v226
	v_cvt_f32_f16_sdwa v195, v226 dst_sel:DWORD dst_unused:UNUSED_PAD src0_sel:WORD_1
	v_cvt_f32_f16_e32 v196, v227
	v_cvt_f32_f16_sdwa v197, v227 dst_sel:DWORD dst_unused:UNUSED_PAD src0_sel:WORD_1
	v_cvt_f32_f16_e32 v190, v228
	v_cvt_f32_f16_sdwa v191, v228 dst_sel:DWORD dst_unused:UNUSED_PAD src0_sel:WORD_1
	v_cvt_f32_f16_e32 v192, v229
	v_cvt_f32_f16_sdwa v193, v229 dst_sel:DWORD dst_unused:UNUSED_PAD src0_sel:WORD_1
	v_cvt_f32_f16_e32 v186, v230
	v_cvt_f32_f16_sdwa v187, v230 dst_sel:DWORD dst_unused:UNUSED_PAD src0_sel:WORD_1
	v_cvt_f32_f16_e32 v188, v231
	v_cvt_f32_f16_sdwa v189, v231 dst_sel:DWORD dst_unused:UNUSED_PAD src0_sel:WORD_1
	s_nop 7
	v_exp_f32_e32 v182, v182
	v_exp_f32_e32 v183, v183
	v_exp_f32_e32 v184, v184
	v_exp_f32_e32 v185, v185
	v_exp_f32_e32 v178, v178
	v_exp_f32_e32 v179, v179
	v_exp_f32_e32 v180, v180
	v_exp_f32_e32 v181, v181
	v_exp_f32_e32 v174, v174
	v_exp_f32_e32 v175, v175
	v_exp_f32_e32 v176, v176
	v_exp_f32_e32 v177, v177
	v_exp_f32_e32 v170, v170
	v_exp_f32_e32 v171, v171
	v_exp_f32_e32 v172, v172
	v_exp_f32_e32 v173, v173
	v_add_f32_e32 v182, 1.0, v182
	v_add_f32_e32 v183, 1.0, v183
	v_add_f32_e32 v184, 1.0, v184
	v_add_f32_e32 v185, 1.0, v185
	v_add_f32_e32 v178, 1.0, v178
	v_add_f32_e32 v179, 1.0, v179
	v_add_f32_e32 v180, 1.0, v180
	v_add_f32_e32 v181, 1.0, v181
	v_add_f32_e32 v174, 1.0, v174
	v_add_f32_e32 v175, 1.0, v175
	v_add_f32_e32 v176, 1.0, v176
	v_add_f32_e32 v177, 1.0, v177
	v_add_f32_e32 v170, 1.0, v170
	v_add_f32_e32 v171, 1.0, v171
	v_add_f32_e32 v172, 1.0, v172
	v_add_f32_e32 v173, 1.0, v173
	v_rcp_f32_e32 v182, v182
	v_rcp_f32_e32 v183, v183
	v_rcp_f32_e32 v184, v184
	v_rcp_f32_e32 v185, v185
	v_rcp_f32_e32 v178, v178
	v_rcp_f32_e32 v179, v179
	v_rcp_f32_e32 v180, v180
	v_rcp_f32_e32 v181, v181
	v_rcp_f32_e32 v174, v174
	v_rcp_f32_e32 v175, v175
	v_rcp_f32_e32 v176, v176
	v_rcp_f32_e32 v177, v177
	v_rcp_f32_e32 v170, v170
	v_rcp_f32_e32 v171, v171
	v_rcp_f32_e32 v172, v172
	v_rcp_f32_e32 v173, v173
	v_fma_f32 v182, v182, -2.0, 1.0
	v_fma_f32 v183, v183, -2.0, 1.0
	v_fma_f32 v184, v184, -2.0, 1.0
	v_fma_f32 v185, v185, -2.0, 1.0
	v_fma_f32 v178, v178, -2.0, 1.0
	v_fma_f32 v179, v179, -2.0, 1.0
	v_fma_f32 v180, v180, -2.0, 1.0
	v_fma_f32 v181, v181, -2.0, 1.0
	v_fma_f32 v174, v174, -2.0, 1.0
	v_fma_f32 v175, v175, -2.0, 1.0
	v_fma_f32 v176, v176, -2.0, 1.0
	v_fma_f32 v177, v177, -2.0, 1.0
	v_fma_f32 v170, v170, -2.0, 1.0
	v_fma_f32 v171, v171, -2.0, 1.0
	v_fma_f32 v172, v172, -2.0, 1.0
	v_fma_f32 v173, v173, -2.0, 1.0
	v_cvt_pk_f16_f32 v182, v182, v183
	v_cvt_pk_f16_f32 v183, v184, v185
	v_cvt_pk_f16_f32 v178, v178, v179
	v_cvt_pk_f16_f32 v179, v180, v181
	v_cvt_pk_f16_f32 v174, v174, v175
	v_cvt_pk_f16_f32 v175, v176, v177
	v_cvt_pk_f16_f32 v170, v170, v171
	v_cvt_pk_f16_f32 v171, v172, v173
	v_add_u32_e32 v244, s5, v210
	ds_write_b64 v244, v[182:183]
	v_add_u32_e32 v245, s5, v1
	ds_write_b64 v245, v[178:179]
	v_add_u32_e32 v246, s5, v216
	ds_write_b64 v246, v[174:175]
	v_add_u32_e32 v247, s5, v214
	ds_write_b64 v247, v[170:171]
	s_addk_i32 s3, 0x4000
	v_lshl_add_u64 v[208:209], v[208:209], 0, s[0:1]
	s_cmp_eq_u32 s3, 0x44000
	s_waitcnt lgkmcnt(0)
	s_barrier
	s_cbranch_scc0 .Lrnn_top
